# hand-written software-pipelined fp8 weight converter (two strip pairs in flight) for the idle workgroups of the mixer phase, on top of v13
# speedup vs baseline: 1.0203x; 1.0203x over previous
.LBB0_486:
	s_or_b64 exec, exec, s[8:9]
	v_readlane_b32 s33, v255, 12
	s_cmpk_lt_u32 s33, 192
	s_cbranch_scc1 .Lfc_p3_skip
	v_lshrrev_b32_e32 v1, 4, v0
	v_lshlrev_b32_e32 v1, 1, v1
	v_and_b32_e32 v2, 15, v0
	v_lshlrev_b32_e32 v2, 4, v2
	v_mov_b32_e32 v3, 0
	v_and_b32_e32 v4, 7, v0
	v_lshlrev_b32_e32 v4, 3, v4
	v_mov_b32_e32 v5, 0
	v_lshrrev_b32_e32 v6, 3, v0
	v_mov_b32_e32 v7, 2
	v_mov_b32_e32 v8, 0x42800000
	v_mov_b32_e32 v9, 0x42800000
	v_and_b32_e32 v16, 15, v0
	v_mul_u32_u24_e32 v16, 0x110, v16
	v_add_u32_e32 v16, v16, v1
	v_mul_u32_u24_e32 v17, 0x44, v6
	v_add_u32_e32 v17, v17, v4
	v_mov_b32_e32 v13, 0x25a00
	v_readlane_b32 s56, v255, 5
	v_readlane_b32 s57, v255, 6
	v_readlane_b32 s13, v255, 7
	v_readlane_b32 s8, v255, 14
	v_readlane_b32 s9, v255, 15
	v_readlane_b32 s33, v255, 18
	s_load_dwordx2 s[36:37], s[8:9], 0x30
	s_load_dwordx2 s[38:39], s[8:9], 0x48
	s_load_dwordx4 s[40:43], s[8:9], 0x78
	s_load_dwordx2 s[44:45], s[8:9], 0x88
	s_add_u32 s58, s56, 0x5000
	s_addc_u32 s59, s57, 0
	s_lshl_b32 s33, s33, 10
	s_add_i32 s33, s33, 512
	s_add_u32 s60, s58, s33
	s_addc_u32 s61, s59, 0
	s_waitcnt lgkmcnt(0)
	v_cmp_eq_u32_e32 vcc, 0, v0
	s_and_saveexec_b64 s[16:17], vcc
	s_cbranch_execz .Lfc_p3_init_done
	global_load_dword v11, v195, s[60:61] sc1
	s_mov_b32 s14, -1
	s_mov_b32 s25, -1
	s_waitcnt vmcnt(0)
	v_readfirstlane_b32 s33, v11
	s_cmp_ge_u32 s33, s13
	s_cbranch_scc1 .Lfc_p3_init_w
	v_mov_b32_e32 v12, 4
	global_atomic_add v10, v195, v12, s[58:59] sc0
	s_waitcnt vmcnt(0)
	v_readfirstlane_b32 s33, v10
	s_cmpk_lt_u32 s33, 0x4c40
	s_cselect_b32 s14, s33, -1
	s_add_i32 s33, s33, 2
	s_cmpk_lt_u32 s33, 0x4c40
	s_cselect_b32 s25, s33, -1
.Lfc_p3_init_w:
	v_mov_b32_e32 v12, s14
	v_mov_b32_e32 v14, s25
	ds_write2_b32 v13, v12, v14 offset1:1
.Lfc_p3_init_done:
	s_or_b64 exec, exec, s[16:17]
	s_waitcnt lgkmcnt(0)
	s_barrier
	ds_read2_b32 v[14:15], v13 offset1:1
	s_waitcnt lgkmcnt(0)
	v_readfirstlane_b32 s14, v14
	v_readfirstlane_b32 s25, v15
	s_cmp_lt_i32 s14, 0
	s_cbranch_scc1 .Lfc_p3_exit
	s_barrier
	s_and_b32 s35, s14, 0x3fffffff
	s_cmpk_ge_u32 s35, 0x2620
	s_cselect_b32 s33, 1, 0
	s_mul_i32 s8, s33, 0x2620
	s_sub_u32 s35, s35, s8
	s_cmpk_lt_u32 s35, 0x420
	s_cbranch_scc1 .Lfc_p3_pro_s0_kin
	s_cmpk_lt_u32 s35, 0x520
	s_cbranch_scc1 .Lfc_p3_pro_s0_kout
	s_cmpk_lt_u32 s35, 0x1b20
	s_cbranch_scc1 .Lfc_p3_pro_s0_kgu
	s_sub_u32 s35, s35, 0x1b20
	s_mul_i32 s8, s35, 0xba2f
	s_lshr_b32 s8, s8, 23
	s_mul_i32 s9, s8, 0xb0
	s_sub_u32 s35, s35, s9
	s_lshl_b32 s33, s33, 4
	s_add_i32 s33, s33, s8
	s_lshr_b32 s8, s35, 1
	s_mul_i32 s9, s8, 0xbb
	s_lshr_b32 s9, s9, 11
	s_mul_i32 s18, s9, 11
	s_sub_u32 s8, s8, s18
	s_lshl_b32 s9, s9, 1
	s_and_b32 s35, s35, 1
	s_or_b32 s9, s9, s35
	s_mov_b64 s[62:63], s[44:45]
	s_movk_i32 s2, 0x2000
	s_movk_i32 s10, 0x600
	s_mul_i32 s18, s33, 0xb00000
	s_mul_i32 s19, s8, 0x100000
	s_add_u32 s18, s18, s19
	s_mul_i32 s19, s33, 0x300000
	s_add_u32 s19, s19, 0x1b300000
	s_mul_i32 s35, s9, 0x30000
	s_add_u32 s19, s19, s35
	s_branch .Lfc_p3_pro_s0_kfin
.Lfc_p3_pro_s0_kin:
	s_lshr_b32 s8, s35, 1
	s_lshr_b32 s9, s8, 4
	s_and_b32 s8, s8, 15
	s_lshl_b32 s9, s9, 1
	s_and_b32 s35, s35, 1
	s_or_b32 s9, s9, s35
	s_mov_b64 s[62:63], s[36:37]
	s_mov_b32 s2, 0x8400
	s_movk_i32 s10, 0x800
	s_mul_i32 s18, s33, 0x4200000
	s_mul_i32 s19, s8, 0x420000
	s_add_u32 s18, s18, s19
	s_mul_i32 s19, s33, 0x2100000
	s_add_u32 s19, s19, 0x100000
	s_lshl_b32 s35, s9, 18
	s_add_u32 s19, s19, s35
	s_branch .Lfc_p3_pro_s0_kfin
.Lfc_p3_pro_s0_kout:
	s_sub_u32 s35, s35, 0x420
	s_lshr_b32 s8, s35, 1
	s_lshr_b32 s9, s8, 4
	s_and_b32 s8, s8, 15
	s_lshl_b32 s9, s9, 1
	s_and_b32 s35, s35, 1
	s_or_b32 s9, s9, s35
	s_mov_b64 s[62:63], s[38:39]
	s_movk_i32 s2, 0x2000
	s_movk_i32 s10, 0x800
	s_lshl_b32 s18, s33, 24
	s_lshl_b32 s19, s8, 20
	s_add_u32 s18, s18, s19
	s_lshl_b32 s19, s33, 23
	s_add_u32 s19, s19, 0x4300000
	s_lshl_b32 s35, s9, 18
	s_add_u32 s19, s19, s35
	s_branch .Lfc_p3_pro_s0_kfin
.Lfc_p3_pro_s0_kgu:
	s_sub_u32 s35, s35, 0x520
	s_mul_i32 s8, s35, 0xba2f
	s_lshr_b32 s8, s8, 23
	s_mul_i32 s9, s8, 0xb0
	s_sub_u32 s35, s35, s9
	s_and_b32 s18, s8, 1
	s_lshr_b32 s8, s8, 1
	s_lshl_b32 s33, s33, 4
	s_add_i32 s33, s33, s8
	s_cmp_eq_u32 s18, 0
	s_cselect_b32 s62, s40, s42
	s_cselect_b32 s63, s41, s43
	s_cmpk_lt_u32 s35, 0xa0
	s_cbranch_scc1 .Lfc_p3_pro_s0_gu_lo
	s_sub_u32 s8, s35, 0xa0
	s_movk_i32 s9, 10
	s_branch .Lfc_p3_pro_s0_gu_j
.Lfc_p3_pro_s0_gu_lo:
	s_lshr_b32 s8, s35, 1
	s_lshr_b32 s9, s8, 4
	s_and_b32 s8, s8, 15
	s_lshl_b32 s9, s9, 1
	s_and_b32 s35, s35, 1
	s_or_b32 s9, s9, s35
.Lfc_p3_pro_s0_gu_j:
	s_movk_i32 s2, 0x1600
	s_movk_i32 s10, 0x800
	s_lshl_b32 s35, s9, 1
	s_add_i32 s35, s35, s18
	s_lshl_b32 s35, s35, 18
	s_mul_i32 s18, s33, 0xb00000
	s_mul_i32 s19, s8, 0xb0000
	s_add_u32 s18, s18, s19
	s_mul_i32 s19, s33, 0x580000
	s_add_u32 s19, s19, 0x5300000
	s_add_u32 s19, s19, s35
.Lfc_p3_pro_s0_kfin:
	s_lshl_b32 s9, s9, 9
	s_add_u32 s18, s18, s9
	s_add_u32 s62, s62, s18
	s_addc_u32 s63, s63, 0
	s_lshl_b32 s8, s8, 7
	s_add_u32 s19, s19, s8
	s_add_u32 s64, s56, s19
	s_addc_u32 s65, s57, 0
	v_mov_b32_e32 v14, s62
	v_mov_b32_e32 v15, s63
	v_lshl_add_u64 v[14:15], v[14:15], 0, v[2:3]
	v_mad_u64_u32 v[20:21], vcc, v1, s2, v[14:15]
	s_lshl_b32 s18, s2, 6
	s_mov_b32 s19, 0
	v_lshl_add_u64 v[22:23], v[20:21], 0, s[2:3]
	v_lshl_add_u64 v[24:25], v[20:21], 0, s[18:19]
	v_lshl_add_u64 v[26:27], v[22:23], 0, s[18:19]
	global_load_dwordx4 v[48:51], v[20:21], off nt
	global_load_dwordx4 v[52:55], v[22:23], off nt
	global_load_dwordx4 v[56:59], v[20:21], off offset:256 nt
	global_load_dwordx4 v[60:63], v[22:23], off offset:256 nt
	global_load_dwordx4 v[64:67], v[24:25], off nt
	global_load_dwordx4 v[68:71], v[26:27], off nt
	global_load_dwordx4 v[72:75], v[24:25], off offset:256 nt
	global_load_dwordx4 v[76:79], v[26:27], off offset:256 nt
	v_mov_b32_e32 v14, s64
	v_mov_b32_e32 v15, s65
	v_lshl_add_u64 v[14:15], v[14:15], 0, v[4:5]
	v_mad_u64_u32 v[28:29], vcc, v6, s10, v[14:15]
	s_lshl_b32 s18, s10, 6
	v_lshl_add_u64 v[30:31], v[28:29], 0, s[18:19]
	s_and_b32 s35, s14, 0x3fffffff
	s_add_i32 s35, s35, 1
	s_cmpk_ge_u32 s35, 0x2620
	s_cselect_b32 s33, 1, 0
	s_mul_i32 s8, s33, 0x2620
	s_sub_u32 s35, s35, s8
	s_cmpk_lt_u32 s35, 0x420
	s_cbranch_scc1 .Lfc_p3_pro_s1_kin
	s_cmpk_lt_u32 s35, 0x520
	s_cbranch_scc1 .Lfc_p3_pro_s1_kout
	s_cmpk_lt_u32 s35, 0x1b20
	s_cbranch_scc1 .Lfc_p3_pro_s1_kgu
	s_sub_u32 s35, s35, 0x1b20
	s_mul_i32 s8, s35, 0xba2f
	s_lshr_b32 s8, s8, 23
	s_mul_i32 s9, s8, 0xb0
	s_sub_u32 s35, s35, s9
	s_lshl_b32 s33, s33, 4
	s_add_i32 s33, s33, s8
	s_lshr_b32 s8, s35, 1
	s_mul_i32 s9, s8, 0xbb
	s_lshr_b32 s9, s9, 11
	s_mul_i32 s18, s9, 11
	s_sub_u32 s8, s8, s18
	s_lshl_b32 s9, s9, 1
	s_and_b32 s35, s35, 1
	s_or_b32 s9, s9, s35
	s_mov_b64 s[62:63], s[44:45]
	s_movk_i32 s2, 0x2000
	s_movk_i32 s10, 0x600
	s_mul_i32 s18, s33, 0xb00000
	s_mul_i32 s19, s8, 0x100000
	s_add_u32 s18, s18, s19
	s_mul_i32 s19, s33, 0x300000
	s_add_u32 s19, s19, 0x1b300000
	s_mul_i32 s35, s9, 0x30000
	s_add_u32 s19, s19, s35
	s_branch .Lfc_p3_pro_s1_kfin

.Lfc_p3_pro_s1_kfin:
	s_lshl_b32 s9, s9, 9
	s_add_u32 s18, s18, s9
	s_add_u32 s62, s62, s18
	s_addc_u32 s63, s63, 0
	s_lshl_b32 s8, s8, 7
	s_add_u32 s19, s19, s8
	s_add_u32 s64, s56, s19
	s_addc_u32 s65, s57, 0
	v_mov_b32_e32 v14, s62
	v_mov_b32_e32 v15, s63
	v_lshl_add_u64 v[14:15], v[14:15], 0, v[2:3]
	v_mad_u64_u32 v[20:21], vcc, v1, s2, v[14:15]
	s_lshl_b32 s18, s2, 6
	s_mov_b32 s19, 0
	v_lshl_add_u64 v[22:23], v[20:21], 0, s[2:3]
	v_lshl_add_u64 v[24:25], v[20:21], 0, s[18:19]
	v_lshl_add_u64 v[26:27], v[22:23], 0, s[18:19]
	global_load_dwordx4 v[80:83], v[20:21], off nt
	global_load_dwordx4 v[84:87], v[22:23], off nt
	global_load_dwordx4 v[88:91], v[20:21], off offset:256 nt
	global_load_dwordx4 v[92:95], v[22:23], off offset:256 nt
	global_load_dwordx4 v[96:99], v[24:25], off nt
	global_load_dwordx4 v[100:103], v[26:27], off nt
	global_load_dwordx4 v[104:107], v[24:25], off offset:256 nt
	global_load_dwordx4 v[108:111], v[26:27], off offset:256 nt
	v_mov_b32_e32 v14, s64
	v_mov_b32_e32 v15, s65
	v_lshl_add_u64 v[14:15], v[14:15], 0, v[4:5]
	v_mad_u64_u32 v[32:33], vcc, v6, s10, v[14:15]
	s_lshl_b32 s18, s10, 6
	v_lshl_add_u64 v[34:35], v[32:33], 0, s[18:19]
.Lfc_p3_top:
	s_cmp_lt_i32 s25, 0
	s_cbranch_scc1 .Lfc_p3_st0_nonext
	s_bitcmp1_b32 s25, 30
	s_cbranch_scc1 .Lfc_p3_st0_noclaim
	v_cmp_eq_u32_e32 vcc, 0, v0
	s_and_saveexec_b64 s[16:17], vcc
	s_cbranch_execz .Lfc_p3_st0_claimed
	global_atomic_add v10, v195, v7, s[58:59] sc0
	global_load_dword v11, v195, s[60:61] sc1

.Lfc_p3_st0_noclaim:
	s_and_b32 s35, s25, 0x3fffffff
	s_cmpk_ge_u32 s35, 0x2620
	s_cselect_b32 s33, 1, 0
	s_mul_i32 s8, s33, 0x2620
	s_sub_u32 s35, s35, s8
	s_cmpk_lt_u32 s35, 0x420
	s_cbranch_scc1 .Lfc_p3_st0_s0_kin
	s_cmpk_lt_u32 s35, 0x520
	s_cbranch_scc1 .Lfc_p3_st0_s0_kout
	s_cmpk_lt_u32 s35, 0x1b20
	s_cbranch_scc1 .Lfc_p3_st0_s0_kgu
	s_sub_u32 s35, s35, 0x1b20
	s_mul_i32 s8, s35, 0xba2f
	s_lshr_b32 s8, s8, 23
	s_mul_i32 s9, s8, 0xb0
	s_sub_u32 s35, s35, s9
	s_lshl_b32 s33, s33, 4
	s_add_i32 s33, s33, s8
	s_lshr_b32 s8, s35, 1
	s_mul_i32 s9, s8, 0xbb
	s_lshr_b32 s9, s9, 11
	s_mul_i32 s18, s9, 11
	s_sub_u32 s8, s8, s18
	s_lshl_b32 s9, s9, 1
	s_and_b32 s35, s35, 1
	s_or_b32 s9, s9, s35
	s_mov_b64 s[62:63], s[44:45]
	s_movk_i32 s2, 0x2000
	s_movk_i32 s10, 0x600
	s_mul_i32 s18, s33, 0xb00000
	s_mul_i32 s19, s8, 0x100000
	s_add_u32 s18, s18, s19
	s_mul_i32 s19, s33, 0x300000
	s_add_u32 s19, s19, 0x1b300000
	s_mul_i32 s35, s9, 0x30000
	s_add_u32 s19, s19, s35
	s_branch .Lfc_p3_st0_s0_kfin

.Lfc_p3_st0_s0_kfin:
	s_lshl_b32 s9, s9, 9
	s_add_u32 s18, s18, s9
	s_add_u32 s62, s62, s18
	s_addc_u32 s63, s63, 0
	s_lshl_b32 s8, s8, 7
	s_add_u32 s19, s19, s8
	s_add_u32 s64, s56, s19
	s_addc_u32 s65, s57, 0
	v_mov_b32_e32 v14, s62
	v_mov_b32_e32 v15, s63
	v_lshl_add_u64 v[14:15], v[14:15], 0, v[2:3]
	v_mad_u64_u32 v[20:21], vcc, v1, s2, v[14:15]
	s_lshl_b32 s18, s2, 6
	s_mov_b32 s19, 0
	v_lshl_add_u64 v[22:23], v[20:21], 0, s[2:3]
	v_lshl_add_u64 v[24:25], v[20:21], 0, s[18:19]
	v_lshl_add_u64 v[26:27], v[22:23], 0, s[18:19]
	global_load_dwordx4 v[112:115], v[20:21], off nt
	global_load_dwordx4 v[116:119], v[22:23], off nt
	global_load_dwordx4 v[120:123], v[20:21], off offset:256 nt
	global_load_dwordx4 v[124:127], v[22:23], off offset:256 nt
	global_load_dwordx4 v[128:131], v[24:25], off nt
	global_load_dwordx4 v[132:135], v[26:27], off nt
	global_load_dwordx4 v[136:139], v[24:25], off offset:256 nt
	global_load_dwordx4 v[140:143], v[26:27], off offset:256 nt
	v_mov_b32_e32 v14, s64
	v_mov_b32_e32 v15, s65
	v_lshl_add_u64 v[14:15], v[14:15], 0, v[4:5]
	v_mad_u64_u32 v[36:37], vcc, v6, s10, v[14:15]
	s_lshl_b32 s18, s10, 6
	v_lshl_add_u64 v[38:39], v[36:37], 0, s[18:19]
	s_and_b32 s35, s25, 0x3fffffff
	s_add_i32 s35, s35, 1
	s_cmpk_ge_u32 s35, 0x2620
	s_cselect_b32 s33, 1, 0
	s_mul_i32 s8, s33, 0x2620
	s_sub_u32 s35, s35, s8
	s_cmpk_lt_u32 s35, 0x420
	s_cbranch_scc1 .Lfc_p3_st0_s1_kin
	s_cmpk_lt_u32 s35, 0x520
	s_cbranch_scc1 .Lfc_p3_st0_s1_kout
	s_cmpk_lt_u32 s35, 0x1b20
	s_cbranch_scc1 .Lfc_p3_st0_s1_kgu
	s_sub_u32 s35, s35, 0x1b20
	s_mul_i32 s8, s35, 0xba2f
	s_lshr_b32 s8, s8, 23
	s_mul_i32 s9, s8, 0xb0
	s_sub_u32 s35, s35, s9
	s_lshl_b32 s33, s33, 4
	s_add_i32 s33, s33, s8
	s_lshr_b32 s8, s35, 1
	s_mul_i32 s9, s8, 0xbb
	s_lshr_b32 s9, s9, 11
	s_mul_i32 s18, s9, 11
	s_sub_u32 s8, s8, s18
	s_lshl_b32 s9, s9, 1
	s_and_b32 s35, s35, 1
	s_or_b32 s9, s9, s35
	s_mov_b64 s[62:63], s[44:45]
	s_movk_i32 s2, 0x2000
	s_movk_i32 s10, 0x600
	s_mul_i32 s18, s33, 0xb00000
	s_mul_i32 s19, s8, 0x100000
	s_add_u32 s18, s18, s19
	s_mul_i32 s19, s33, 0x300000
	s_add_u32 s19, s19, 0x1b300000
	s_mul_i32 s35, s9, 0x30000
	s_add_u32 s19, s19, s35
	s_branch .Lfc_p3_st0_s1_kfin

.Lfc_p3_st0_s1_kfin:
	s_lshl_b32 s9, s9, 9
	s_add_u32 s18, s18, s9
	s_add_u32 s62, s62, s18
	s_addc_u32 s63, s63, 0
	s_lshl_b32 s8, s8, 7
	s_add_u32 s19, s19, s8
	s_add_u32 s64, s56, s19
	s_addc_u32 s65, s57, 0
	v_mov_b32_e32 v14, s62
	v_mov_b32_e32 v15, s63
	v_lshl_add_u64 v[14:15], v[14:15], 0, v[2:3]
	v_mad_u64_u32 v[20:21], vcc, v1, s2, v[14:15]
	s_lshl_b32 s18, s2, 6
	s_mov_b32 s19, 0
	v_lshl_add_u64 v[22:23], v[20:21], 0, s[2:3]
	v_lshl_add_u64 v[24:25], v[20:21], 0, s[18:19]
	v_lshl_add_u64 v[26:27], v[22:23], 0, s[18:19]
	global_load_dwordx4 v[144:147], v[20:21], off nt
	global_load_dwordx4 v[148:151], v[22:23], off nt
	global_load_dwordx4 v[152:155], v[20:21], off offset:256 nt
	global_load_dwordx4 v[156:159], v[22:23], off offset:256 nt
	global_load_dwordx4 v[160:163], v[24:25], off nt
	global_load_dwordx4 v[164:167], v[26:27], off nt
	global_load_dwordx4 v[168:171], v[24:25], off offset:256 nt
	global_load_dwordx4 v[172:175], v[26:27], off offset:256 nt
	v_mov_b32_e32 v14, s64
	v_mov_b32_e32 v15, s65
	v_lshl_add_u64 v[14:15], v[14:15], 0, v[4:5]
	v_mad_u64_u32 v[40:41], vcc, v6, s10, v[14:15]
	s_lshl_b32 s18, s10, 6
	v_lshl_add_u64 v[42:43], v[40:41], 0, s[18:19]
	s_waitcnt vmcnt(16)
	s_branch .Lfc_p3_st0_cvt

.Lfc_p3_st0_cvt:
	v_pk_mul_f32 v[48:49], v[48:49], v[8:9]
	v_pk_mul_f32 v[50:51], v[50:51], v[8:9]
	v_pk_mul_f32 v[52:53], v[52:53], v[8:9]
	v_pk_mul_f32 v[54:55], v[54:55], v[8:9]
	v_cvt_pk_fp8_f32 v48, v48, v52
	v_cvt_pk_fp8_f32 v49, v49, v53
	v_cvt_pk_fp8_f32 v50, v50, v54
	v_cvt_pk_fp8_f32 v51, v51, v55
	ds_write_b16 v16, v48 offset:0
	ds_write_b16 v16, v49 offset:68
	ds_write_b16 v16, v50 offset:136
	ds_write_b16 v16, v51 offset:204
	v_pk_mul_f32 v[56:57], v[56:57], v[8:9]
	v_pk_mul_f32 v[58:59], v[58:59], v[8:9]
	v_pk_mul_f32 v[60:61], v[60:61], v[8:9]
	v_pk_mul_f32 v[62:63], v[62:63], v[8:9]
	v_cvt_pk_fp8_f32 v56, v56, v60
	v_cvt_pk_fp8_f32 v57, v57, v61
	v_cvt_pk_fp8_f32 v58, v58, v62
	v_cvt_pk_fp8_f32 v59, v59, v63
	ds_write_b16 v16, v56 offset:4352
	ds_write_b16 v16, v57 offset:4420
	ds_write_b16 v16, v58 offset:4488
	ds_write_b16 v16, v59 offset:4556
	v_pk_mul_f32 v[64:65], v[64:65], v[8:9]
	v_pk_mul_f32 v[66:67], v[66:67], v[8:9]
	v_pk_mul_f32 v[68:69], v[68:69], v[8:9]
	v_pk_mul_f32 v[70:71], v[70:71], v[8:9]
	v_cvt_pk_fp8_f32 v64, v64, v68
	v_cvt_pk_fp8_f32 v65, v65, v69
	v_cvt_pk_fp8_f32 v66, v66, v70
	v_cvt_pk_fp8_f32 v67, v67, v71
	ds_write_b16 v16, v64 offset:8704
	ds_write_b16 v16, v65 offset:8772
	ds_write_b16 v16, v66 offset:8840
	ds_write_b16 v16, v67 offset:8908
	v_pk_mul_f32 v[72:73], v[72:73], v[8:9]
	v_pk_mul_f32 v[74:75], v[74:75], v[8:9]
	v_pk_mul_f32 v[76:77], v[76:77], v[8:9]
	v_pk_mul_f32 v[78:79], v[78:79], v[8:9]
	v_cvt_pk_fp8_f32 v72, v72, v76
	v_cvt_pk_fp8_f32 v73, v73, v77
	v_cvt_pk_fp8_f32 v74, v74, v78
	v_cvt_pk_fp8_f32 v75, v75, v79
	ds_write_b16 v16, v72 offset:13056
	ds_write_b16 v16, v73 offset:13124
	ds_write_b16 v16, v74 offset:13192
	ds_write_b16 v16, v75 offset:13260
	v_pk_mul_f32 v[80:81], v[80:81], v[8:9]
	v_pk_mul_f32 v[82:83], v[82:83], v[8:9]
	v_pk_mul_f32 v[84:85], v[84:85], v[8:9]
	v_pk_mul_f32 v[86:87], v[86:87], v[8:9]
	v_cvt_pk_fp8_f32 v80, v80, v84
	v_cvt_pk_fp8_f32 v81, v81, v85
	v_cvt_pk_fp8_f32 v82, v82, v86
	v_cvt_pk_fp8_f32 v83, v83, v87
	ds_write_b16 v16, v80 offset:17408
	ds_write_b16 v16, v81 offset:17476
	ds_write_b16 v16, v82 offset:17544
	ds_write_b16 v16, v83 offset:17612
	v_pk_mul_f32 v[88:89], v[88:89], v[8:9]
	v_pk_mul_f32 v[90:91], v[90:91], v[8:9]
	v_pk_mul_f32 v[92:93], v[92:93], v[8:9]
	v_pk_mul_f32 v[94:95], v[94:95], v[8:9]
	v_cvt_pk_fp8_f32 v88, v88, v92
	v_cvt_pk_fp8_f32 v89, v89, v93
	v_cvt_pk_fp8_f32 v90, v90, v94
	v_cvt_pk_fp8_f32 v91, v91, v95
	ds_write_b16 v16, v88 offset:21760
	ds_write_b16 v16, v89 offset:21828
	ds_write_b16 v16, v90 offset:21896
	ds_write_b16 v16, v91 offset:21964
	v_pk_mul_f32 v[96:97], v[96:97], v[8:9]
	v_pk_mul_f32 v[98:99], v[98:99], v[8:9]
	v_pk_mul_f32 v[100:101], v[100:101], v[8:9]
	v_pk_mul_f32 v[102:103], v[102:103], v[8:9]
	v_cvt_pk_fp8_f32 v96, v96, v100
	v_cvt_pk_fp8_f32 v97, v97, v101
	v_cvt_pk_fp8_f32 v98, v98, v102
	v_cvt_pk_fp8_f32 v99, v99, v103
	ds_write_b16 v16, v96 offset:26112
	ds_write_b16 v16, v97 offset:26180
	ds_write_b16 v16, v98 offset:26248
	ds_write_b16 v16, v99 offset:26316
	v_pk_mul_f32 v[104:105], v[104:105], v[8:9]
	v_pk_mul_f32 v[106:107], v[106:107], v[8:9]
	v_pk_mul_f32 v[108:109], v[108:109], v[8:9]
	v_pk_mul_f32 v[110:111], v[110:111], v[8:9]
	v_cvt_pk_fp8_f32 v104, v104, v108
	v_cvt_pk_fp8_f32 v105, v105, v109
	v_cvt_pk_fp8_f32 v106, v106, v110
	v_cvt_pk_fp8_f32 v107, v107, v111
	ds_write_b16 v16, v104 offset:30464
	ds_write_b16 v16, v105 offset:30532
	ds_write_b16 v16, v106 offset:30600
	ds_write_b16 v16, v107 offset:30668
	v_cmp_eq_u32_e32 vcc, 0, v0
	s_and_saveexec_b64 s[16:17], vcc
	s_cbranch_execz .Lfc_p3_st0_slot_done
	s_mov_b32 s33, -1
	s_cmp_lt_i32 s25, 0
	s_cbranch_scc1 .Lfc_p3_st0_slot_w
	s_bitcmp1_b32 s25, 30
	s_cbranch_scc1 .Lfc_p3_st0_slot_w
	v_readfirstlane_b32 s35, v10
	v_readfirstlane_b32 s8, v11
	s_cmpk_ge_u32 s35, 0x4c40
	s_cbranch_scc1 .Lfc_p3_st0_slot_w
	s_cmp_ge_u32 s8, s13
	s_cselect_b32 s8, 0x40000000, 0
	s_or_b32 s33, s35, s8
.Lfc_p3_st0_slot_w:
	v_mov_b32_e32 v12, s33
	ds_write_b32 v13, v12 offset:0
.Lfc_p3_st0_slot_done:
	s_or_b64 exec, exec, s[16:17]
	s_waitcnt lgkmcnt(0)
	s_barrier
	ds_read_b32 v12, v13 offset:0
	v_add_u32_e32 v176, 0x0, v17
	ds_read2_b32 v[178:179], v176 offset1:1
	v_add_u32_e32 v180, 0x1100, v17
	ds_read2_b32 v[182:183], v180 offset1:1
	v_add_u32_e32 v184, 0x2200, v17
	ds_read2_b32 v[186:187], v184 offset1:1
	v_add_u32_e32 v188, 0x3300, v17
	ds_read2_b32 v[190:191], v188 offset1:1
	s_waitcnt lgkmcnt(3)
	global_store_dwordx2 v[28:29], v[178:179], off
	s_waitcnt lgkmcnt(2)
	global_store_dwordx2 v[30:31], v[182:183], off
	s_waitcnt lgkmcnt(1)
	global_store_dwordx2 v[28:29], v[186:187], off offset:64
	s_waitcnt lgkmcnt(0)
	global_store_dwordx2 v[30:31], v[190:191], off offset:64
	v_add_u32_e32 v176, 0x4400, v17
	ds_read2_b32 v[178:179], v176 offset1:1
	v_add_u32_e32 v180, 0x5500, v17
	ds_read2_b32 v[182:183], v180 offset1:1
	v_add_u32_e32 v184, 0x6600, v17
	ds_read2_b32 v[186:187], v184 offset1:1
	v_add_u32_e32 v188, 0x7700, v17
	ds_read2_b32 v[190:191], v188 offset1:1
	s_waitcnt lgkmcnt(3)
	global_store_dwordx2 v[32:33], v[178:179], off
	s_waitcnt lgkmcnt(2)
	global_store_dwordx2 v[34:35], v[182:183], off
	s_waitcnt lgkmcnt(1)
	global_store_dwordx2 v[32:33], v[186:187], off offset:64
	s_waitcnt lgkmcnt(0)
	global_store_dwordx2 v[34:35], v[190:191], off offset:64
	s_waitcnt lgkmcnt(0)
	s_mov_b32 s14, s25
	v_readfirstlane_b32 s25, v12
	s_cmp_lt_i32 s14, 0
	s_cbranch_scc1 .Lfc_p3_exit
	s_cmp_lt_i32 s25, 0
	s_cbranch_scc1 .Lfc_p3_st1_nonext
	s_bitcmp1_b32 s25, 30
	s_cbranch_scc1 .Lfc_p3_st1_noclaim
	v_cmp_eq_u32_e32 vcc, 0, v0
	s_and_saveexec_b64 s[16:17], vcc
	s_cbranch_execz .Lfc_p3_st1_claimed
	global_atomic_add v10, v195, v7, s[58:59] sc0
	global_load_dword v11, v195, s[60:61] sc1

.Lfc_p3_st1_s0_kfin:
	s_lshl_b32 s9, s9, 9
	s_add_u32 s18, s18, s9
	s_add_u32 s62, s62, s18
	s_addc_u32 s63, s63, 0
	s_lshl_b32 s8, s8, 7
	s_add_u32 s19, s19, s8
	s_add_u32 s64, s56, s19
	s_addc_u32 s65, s57, 0
	v_mov_b32_e32 v14, s62
	v_mov_b32_e32 v15, s63
	v_lshl_add_u64 v[14:15], v[14:15], 0, v[2:3]
	v_mad_u64_u32 v[20:21], vcc, v1, s2, v[14:15]
	s_lshl_b32 s18, s2, 6
	s_mov_b32 s19, 0
	v_lshl_add_u64 v[22:23], v[20:21], 0, s[2:3]
	v_lshl_add_u64 v[24:25], v[20:21], 0, s[18:19]
	v_lshl_add_u64 v[26:27], v[22:23], 0, s[18:19]
	global_load_dwordx4 v[48:51], v[20:21], off nt
	global_load_dwordx4 v[52:55], v[22:23], off nt
	global_load_dwordx4 v[56:59], v[20:21], off offset:256 nt
	global_load_dwordx4 v[60:63], v[22:23], off offset:256 nt
	global_load_dwordx4 v[64:67], v[24:25], off nt
	global_load_dwordx4 v[68:71], v[26:27], off nt
	global_load_dwordx4 v[72:75], v[24:25], off offset:256 nt
	global_load_dwordx4 v[76:79], v[26:27], off offset:256 nt
	v_mov_b32_e32 v14, s64
	v_mov_b32_e32 v15, s65
	v_lshl_add_u64 v[14:15], v[14:15], 0, v[4:5]
	v_mad_u64_u32 v[28:29], vcc, v6, s10, v[14:15]
	s_lshl_b32 s18, s10, 6
	v_lshl_add_u64 v[30:31], v[28:29], 0, s[18:19]
	s_and_b32 s35, s25, 0x3fffffff
	s_add_i32 s35, s35, 1
	s_cmpk_ge_u32 s35, 0x2620
	s_cselect_b32 s33, 1, 0
	s_mul_i32 s8, s33, 0x2620
	s_sub_u32 s35, s35, s8
	s_cmpk_lt_u32 s35, 0x420
	s_cbranch_scc1 .Lfc_p3_st1_s1_kin
	s_cmpk_lt_u32 s35, 0x520
	s_cbranch_scc1 .Lfc_p3_st1_s1_kout
	s_cmpk_lt_u32 s35, 0x1b20
	s_cbranch_scc1 .Lfc_p3_st1_s1_kgu
	s_sub_u32 s35, s35, 0x1b20
	s_mul_i32 s8, s35, 0xba2f
	s_lshr_b32 s8, s8, 23
	s_mul_i32 s9, s8, 0xb0
	s_sub_u32 s35, s35, s9
	s_lshl_b32 s33, s33, 4
	s_add_i32 s33, s33, s8
	s_lshr_b32 s8, s35, 1
	s_mul_i32 s9, s8, 0xbb
	s_lshr_b32 s9, s9, 11
	s_mul_i32 s18, s9, 11
	s_sub_u32 s8, s8, s18
	s_lshl_b32 s9, s9, 1
	s_and_b32 s35, s35, 1
	s_or_b32 s9, s9, s35
	s_mov_b64 s[62:63], s[44:45]
	s_movk_i32 s2, 0x2000
	s_movk_i32 s10, 0x600
	s_mul_i32 s18, s33, 0xb00000
	s_mul_i32 s19, s8, 0x100000
	s_add_u32 s18, s18, s19
	s_mul_i32 s19, s33, 0x300000
	s_add_u32 s19, s19, 0x1b300000
	s_mul_i32 s35, s9, 0x30000
	s_add_u32 s19, s19, s35
	s_branch .Lfc_p3_st1_s1_kfin

.Lfc_p3_st1_s1_kfin:
	s_lshl_b32 s9, s9, 9
	s_add_u32 s18, s18, s9
	s_add_u32 s62, s62, s18
	s_addc_u32 s63, s63, 0
	s_lshl_b32 s8, s8, 7
	s_add_u32 s19, s19, s8
	s_add_u32 s64, s56, s19
	s_addc_u32 s65, s57, 0
	v_mov_b32_e32 v14, s62
	v_mov_b32_e32 v15, s63
	v_lshl_add_u64 v[14:15], v[14:15], 0, v[2:3]
	v_mad_u64_u32 v[20:21], vcc, v1, s2, v[14:15]
	s_lshl_b32 s18, s2, 6
	s_mov_b32 s19, 0
	v_lshl_add_u64 v[22:23], v[20:21], 0, s[2:3]
	v_lshl_add_u64 v[24:25], v[20:21], 0, s[18:19]
	v_lshl_add_u64 v[26:27], v[22:23], 0, s[18:19]
	global_load_dwordx4 v[80:83], v[20:21], off nt
	global_load_dwordx4 v[84:87], v[22:23], off nt
	global_load_dwordx4 v[88:91], v[20:21], off offset:256 nt
	global_load_dwordx4 v[92:95], v[22:23], off offset:256 nt
	global_load_dwordx4 v[96:99], v[24:25], off nt
	global_load_dwordx4 v[100:103], v[26:27], off nt
	global_load_dwordx4 v[104:107], v[24:25], off offset:256 nt
	global_load_dwordx4 v[108:111], v[26:27], off offset:256 nt
	v_mov_b32_e32 v14, s64
	v_mov_b32_e32 v15, s65
	v_lshl_add_u64 v[14:15], v[14:15], 0, v[4:5]
	v_mad_u64_u32 v[32:33], vcc, v6, s10, v[14:15]
	s_lshl_b32 s18, s10, 6
	v_lshl_add_u64 v[34:35], v[32:33], 0, s[18:19]
	s_waitcnt vmcnt(16)
	s_branch .Lfc_p3_st1_cvt

.Lfc_p3_st1_cvt:
	v_pk_mul_f32 v[112:113], v[112:113], v[8:9]
	v_pk_mul_f32 v[114:115], v[114:115], v[8:9]
	v_pk_mul_f32 v[116:117], v[116:117], v[8:9]
	v_pk_mul_f32 v[118:119], v[118:119], v[8:9]
	v_cvt_pk_fp8_f32 v112, v112, v116
	v_cvt_pk_fp8_f32 v113, v113, v117
	v_cvt_pk_fp8_f32 v114, v114, v118
	v_cvt_pk_fp8_f32 v115, v115, v119
	ds_write_b16 v16, v112 offset:34816
	ds_write_b16 v16, v113 offset:34884
	ds_write_b16 v16, v114 offset:34952
	ds_write_b16 v16, v115 offset:35020
	v_pk_mul_f32 v[120:121], v[120:121], v[8:9]
	v_pk_mul_f32 v[122:123], v[122:123], v[8:9]
	v_pk_mul_f32 v[124:125], v[124:125], v[8:9]
	v_pk_mul_f32 v[126:127], v[126:127], v[8:9]
	v_cvt_pk_fp8_f32 v120, v120, v124
	v_cvt_pk_fp8_f32 v121, v121, v125
	v_cvt_pk_fp8_f32 v122, v122, v126
	v_cvt_pk_fp8_f32 v123, v123, v127
	ds_write_b16 v16, v120 offset:39168
	ds_write_b16 v16, v121 offset:39236
	ds_write_b16 v16, v122 offset:39304
	ds_write_b16 v16, v123 offset:39372
	v_pk_mul_f32 v[128:129], v[128:129], v[8:9]
	v_pk_mul_f32 v[130:131], v[130:131], v[8:9]
	v_pk_mul_f32 v[132:133], v[132:133], v[8:9]
	v_pk_mul_f32 v[134:135], v[134:135], v[8:9]
	v_cvt_pk_fp8_f32 v128, v128, v132
	v_cvt_pk_fp8_f32 v129, v129, v133
	v_cvt_pk_fp8_f32 v130, v130, v134
	v_cvt_pk_fp8_f32 v131, v131, v135
	ds_write_b16 v16, v128 offset:43520
	ds_write_b16 v16, v129 offset:43588
	ds_write_b16 v16, v130 offset:43656
	ds_write_b16 v16, v131 offset:43724
	v_pk_mul_f32 v[136:137], v[136:137], v[8:9]
	v_pk_mul_f32 v[138:139], v[138:139], v[8:9]
	v_pk_mul_f32 v[140:141], v[140:141], v[8:9]
	v_pk_mul_f32 v[142:143], v[142:143], v[8:9]
	v_cvt_pk_fp8_f32 v136, v136, v140
	v_cvt_pk_fp8_f32 v137, v137, v141
	v_cvt_pk_fp8_f32 v138, v138, v142
	v_cvt_pk_fp8_f32 v139, v139, v143
	ds_write_b16 v16, v136 offset:47872
	ds_write_b16 v16, v137 offset:47940
	ds_write_b16 v16, v138 offset:48008
	ds_write_b16 v16, v139 offset:48076
	v_pk_mul_f32 v[144:145], v[144:145], v[8:9]
	v_pk_mul_f32 v[146:147], v[146:147], v[8:9]
	v_pk_mul_f32 v[148:149], v[148:149], v[8:9]
	v_pk_mul_f32 v[150:151], v[150:151], v[8:9]
	v_cvt_pk_fp8_f32 v144, v144, v148
	v_cvt_pk_fp8_f32 v145, v145, v149
	v_cvt_pk_fp8_f32 v146, v146, v150
	v_cvt_pk_fp8_f32 v147, v147, v151
	ds_write_b16 v16, v144 offset:52224
	ds_write_b16 v16, v145 offset:52292
	ds_write_b16 v16, v146 offset:52360
	ds_write_b16 v16, v147 offset:52428
	v_pk_mul_f32 v[152:153], v[152:153], v[8:9]
	v_pk_mul_f32 v[154:155], v[154:155], v[8:9]
	v_pk_mul_f32 v[156:157], v[156:157], v[8:9]
	v_pk_mul_f32 v[158:159], v[158:159], v[8:9]
	v_cvt_pk_fp8_f32 v152, v152, v156
	v_cvt_pk_fp8_f32 v153, v153, v157
	v_cvt_pk_fp8_f32 v154, v154, v158
	v_cvt_pk_fp8_f32 v155, v155, v159
	ds_write_b16 v16, v152 offset:56576
	ds_write_b16 v16, v153 offset:56644
	ds_write_b16 v16, v154 offset:56712
	ds_write_b16 v16, v155 offset:56780
	v_pk_mul_f32 v[160:161], v[160:161], v[8:9]
	v_pk_mul_f32 v[162:163], v[162:163], v[8:9]
	v_pk_mul_f32 v[164:165], v[164:165], v[8:9]
	v_pk_mul_f32 v[166:167], v[166:167], v[8:9]
	v_cvt_pk_fp8_f32 v160, v160, v164
	v_cvt_pk_fp8_f32 v161, v161, v165
	v_cvt_pk_fp8_f32 v162, v162, v166
	v_cvt_pk_fp8_f32 v163, v163, v167
	ds_write_b16 v16, v160 offset:60928
	ds_write_b16 v16, v161 offset:60996
	ds_write_b16 v16, v162 offset:61064
	ds_write_b16 v16, v163 offset:61132
	v_pk_mul_f32 v[168:169], v[168:169], v[8:9]
	v_pk_mul_f32 v[170:171], v[170:171], v[8:9]
	v_pk_mul_f32 v[172:173], v[172:173], v[8:9]
	v_pk_mul_f32 v[174:175], v[174:175], v[8:9]
	v_cvt_pk_fp8_f32 v168, v168, v172
	v_cvt_pk_fp8_f32 v169, v169, v173
	v_cvt_pk_fp8_f32 v170, v170, v174
	v_cvt_pk_fp8_f32 v171, v171, v175
	ds_write_b16 v16, v168 offset:65280
	ds_write_b16 v16, v169 offset:65348
	ds_write_b16 v16, v170 offset:65416
	ds_write_b16 v16, v171 offset:65484
	v_cmp_eq_u32_e32 vcc, 0, v0
	s_and_saveexec_b64 s[16:17], vcc
	s_cbranch_execz .Lfc_p3_st1_slot_done
	s_mov_b32 s33, -1
	s_cmp_lt_i32 s25, 0
	s_cbranch_scc1 .Lfc_p3_st1_slot_w
	s_bitcmp1_b32 s25, 30
	s_cbranch_scc1 .Lfc_p3_st1_slot_w
	v_readfirstlane_b32 s35, v10
	v_readfirstlane_b32 s8, v11
	s_cmpk_ge_u32 s35, 0x4c40
	s_cbranch_scc1 .Lfc_p3_st1_slot_w
	s_cmp_ge_u32 s8, s13
	s_cselect_b32 s8, 0x40000000, 0
	s_or_b32 s33, s35, s8
.Lfc_p3_st1_slot_w:
	v_mov_b32_e32 v12, s33
	ds_write_b32 v13, v12 offset:4
.Lfc_p3_st1_slot_done:
	s_or_b64 exec, exec, s[16:17]
	s_waitcnt lgkmcnt(0)
	s_barrier
	ds_read_b32 v12, v13 offset:4
	v_add_u32_e32 v176, 0x8800, v17
	ds_read2_b32 v[178:179], v176 offset1:1
	v_add_u32_e32 v180, 0x9900, v17
	ds_read2_b32 v[182:183], v180 offset1:1
	v_add_u32_e32 v184, 0xaa00, v17
	ds_read2_b32 v[186:187], v184 offset1:1
	v_add_u32_e32 v188, 0xbb00, v17
	ds_read2_b32 v[190:191], v188 offset1:1
	s_waitcnt lgkmcnt(3)
	global_store_dwordx2 v[36:37], v[178:179], off
	s_waitcnt lgkmcnt(2)
	global_store_dwordx2 v[38:39], v[182:183], off
	s_waitcnt lgkmcnt(1)
	global_store_dwordx2 v[36:37], v[186:187], off offset:64
	s_waitcnt lgkmcnt(0)
	global_store_dwordx2 v[38:39], v[190:191], off offset:64
	v_add_u32_e32 v176, 0xcc00, v17
	ds_read2_b32 v[178:179], v176 offset1:1
	v_add_u32_e32 v180, 0xdd00, v17
	ds_read2_b32 v[182:183], v180 offset1:1
	v_add_u32_e32 v184, 0xee00, v17
	ds_read2_b32 v[186:187], v184 offset1:1
	v_add_u32_e32 v188, 0xff00, v17
	ds_read2_b32 v[190:191], v188 offset1:1
	s_waitcnt lgkmcnt(3)
	global_store_dwordx2 v[40:41], v[178:179], off
	s_waitcnt lgkmcnt(2)
	global_store_dwordx2 v[42:43], v[182:183], off
	s_waitcnt lgkmcnt(1)
	global_store_dwordx2 v[40:41], v[186:187], off offset:64
	s_waitcnt lgkmcnt(0)
	global_store_dwordx2 v[42:43], v[190:191], off offset:64
	s_waitcnt lgkmcnt(0)
	s_mov_b32 s14, s25
	v_readfirstlane_b32 s25, v12
	s_cmp_lt_i32 s14, 0
	s_cbranch_scc1 .Lfc_p3_exit
	s_branch .Lfc_p3_top
.Lfc_p3_exit:
	s_branch .LBB0_542
.Lfc_p3_skip:
	v_mov_b32_e32 v2, v0
	s_nop 0
	v_cmp_eq_u32_e64 s[40:41], 0, v2
	s_and_saveexec_b64 s[8:9], s[40:41]
	s_cbranch_execz .LBB0_492
	global_load_dword v3, v195, s[26:27] offset:512 sc1
	v_mov_b32_e32 v1, -1
	s_waitcnt vmcnt(0)
	v_cmp_le_u32_e32 vcc, s81, v3
	s_cbranch_vccnz .LBB0_491
	s_mov_b64 s[36:37], exec
	v_mbcnt_lo_u32_b32 v1, s36, 0
	v_mbcnt_hi_u32_b32 v1, s37, v1
	v_cmp_eq_u32_e32 vcc, 0, v1
	s_and_saveexec_b64 s[28:29], vcc
	s_cbranch_execz .LBB0_490
	s_bcnt1_i32_b64 s0, s[36:37]
	s_lshl_b32 s0, s0, 1
	v_mov_b32_e32 v3, s0
	global_atomic_add v3, v195, v3, s[6:7] sc0
